# cfgE + conversion re-split: PRO skips dense FFN weights (moved to H0-shadow with experts 0-1), expert 2 converted in REC by spare WGs (bx>=230 and the 16 S5-scan WGs), REC main group 150 WGs experts 3
# baseline (speedup 1.0000x reference)
.LBB0_15:
	s_cmp_eq_u32 s99, 2
	s_cbranch_scc1 .Ltr_fwd1
	v_lshlrev_b32_e32 v67, 2, v0
	v_and_b32_e32 v71, 60, v67
	v_bfe_u32 v93, v0, 4, 2
	v_lshlrev_b32_e32 v1, 2, v71
	v_mul_u32_u24_e32 v2, 0x104, v93
	v_add3_u32 v73, v31, v1, v2
	v_lshlrev_b32_e32 v1, 3, v0
	v_and_b32_e32 v2, 56, v1
	v_mul_u32_u24_e32 v3, 0x104, v2
	v_lshlrev_b32_e32 v4, 2, v66
	s_movk_i32 s0, 0x400
	v_mov_b32_e32 v77, 0
	v_add3_u32 v88, v31, v3, v4
	v_or_b32_e32 v89, 32, v66
	v_or_b32_e32 v90, 40, v66
	v_or_b32_e32 v91, 48, v66
	v_or_b32_e32 v92, 56, v66
	v_cmp_gt_i32_e64 s[6:7], s0, v69
	v_lshlrev_b32_e32 v76, 1, v2
	v_lshlrev_b32_e32 v94, 6, v186
	s_cmp_eq_u32 s99, 0
	s_cselect_b64 vcc, s[6:7], 0
	s_and_saveexec_b64 s[0:1], vcc
	s_cbranch_execz .LBB0_50
	v_lshl_add_u64 v[2:3], s[58:59], 0, v[76:77]
	s_mov_b64 s[8:9], 0x3da00000
	v_lshl_add_u64 v[82:83], v[2:3], 0, s[8:9]
	v_lshl_or_b32 v77, s96, 9, v94
	s_lshl_b32 s14, s3, 6
	s_mov_b64 s[8:9], 0
	s_movk_i32 s15, 0x800
	s_movk_i32 s16, 0x3ff
	v_mov_b32_e32 v95, v69
	s_branch .LBB0_18

.LBB0_50:
	s_or_b64 exec, exec, s[0:1]
	s_movk_i32 s0, 0x100
	v_cmp_gt_i32_e32 vcc, s0, v69
	s_cmp_eq_u32 s99, 0
	s_cselect_b64 vcc, vcc, 0
	s_and_saveexec_b64 s[0:1], vcc
	s_cbranch_execz .LBB0_85
	v_mov_b32_e32 v77, 0
	v_lshl_add_u64 v[2:3], s[58:59], 0, v[76:77]
	s_mov_b64 s[8:9], 0x3d800000
	v_lshl_add_u64 v[82:83], v[2:3], 0, s[8:9]
	v_lshl_or_b32 v77, s96, 9, v94
	s_lshl_b32 s14, s3, 6
	s_mov_b64 s[8:9], 0
	s_movk_i32 s15, 0x400
	s_movk_i32 s16, 0xff
	v_mov_b32_e32 v95, v69
	s_branch .LBB0_53

.LBB0_85:
	s_or_b64 exec, exec, s[0:1]
	s_movk_i32 s0, 0xa80
	v_cmp_gt_i32_e32 vcc, s0, v69
	s_cmp_eq_u32 s99, 0
	s_cselect_b64 vcc, vcc, 0
	s_and_saveexec_b64 s[0:1], vcc
	s_cbranch_execz .LBB0_120
	v_mov_b32_e32 v77, 0
	v_lshl_add_u64 v[2:3], s[58:59], 0, v[76:77]
	s_mov_b64 s[8:9], 0x3c300000
	v_lshl_or_b32 v77, s96, 9, v94
	v_lshl_add_u64 v[82:83], v[2:3], 0, s[8:9]
	v_or_b32_e32 v2, v77, v93
	s_movk_i32 s17, 0x1410
	s_lshl_b32 s16, s3, 6
	v_mul_lo_u32 v84, v2, s17
	s_mul_i32 s18, s3, 0x50400
	s_mov_b64 s[12:13], 0
	s_mov_b32 s19, 0xff5f8000
	s_movk_i32 s21, 0xa7f
	v_mov_b32_e32 v85, v69
	s_branch .LBB0_88

.LBB0_120:
	s_or_b64 exec, exec, s[0:1]
	s_movk_i32 s0, 0xb00
	v_cmp_gt_i32_e32 vcc, s0, v69
	s_cmp_eq_u32 s99, 1
	s_cselect_b64 vcc, vcc, 0
	s_and_saveexec_b64 s[0:1], vcc
	s_cbranch_execz .LBB0_191
	v_lshlrev_b32_e32 v2, 2, v78
	v_mov_b32_e32 v3, 0
	v_lshl_add_u64 v[18:19], s[50:51], 0, v[2:3]
	v_mul_u32_u24_e32 v2, 0x84, v66
	s_mov_b64 s[8:9], 0x3ad00000
	v_add_u32_e32 v30, v79, v2
	v_lshl_add_u64 v[20:21], v[80:81], 0, s[8:9]
	s_lshl_b32 s12, s3, 7
	s_mov_b64 s[8:9], 0
	s_mov_b32 s13, 0x2e8ba2e9
	s_movk_i32 s14, 0xea00
	v_add_u32_e32 v31, 0x420, v30
	v_add_u32_e32 v32, 0x428, v30
	v_add_u32_e32 v33, 0x840, v30
	v_add_u32_e32 v34, 0x848, v30
	v_add_u32_e32 v35, 0xc60, v30
	v_add_u32_e32 v36, 0xc68, v30
	v_add_u32_e32 v37, 0x1080, v30
	v_add_u32_e32 v38, 0x1088, v30
	v_add_u32_e32 v39, 0x14a0, v30
	v_add_u32_e32 v40, 0x14a8, v30
	v_add_u32_e32 v41, 0x18c0, v30
	v_add_u32_e32 v42, 0x18c8, v30
	v_add_u32_e32 v43, 0x1ce0, v30
	v_add_u32_e32 v44, 0x1ce8, v30
	v_add_u32_e32 v45, 0x2100, v30
	v_add_u32_e32 v46, 0x2108, v30
	v_add_u32_e32 v47, 0x2520, v30
	v_add_u32_e32 v48, 0x2528, v30
	v_add_u32_e32 v49, 0x2940, v30
	v_add_u32_e32 v50, 0x2948, v30
	v_add_u32_e32 v51, 0x2d60, v30
	v_add_u32_e32 v52, 0x2d68, v30
	v_add_u32_e32 v53, 0x3180, v30
	v_add_u32_e32 v54, 0x3188, v30
	v_add_u32_e32 v55, 0x35a0, v30
	v_add_u32_e32 v56, 0x35a8, v30
	v_add_u32_e32 v57, 0x39c0, v30
	v_add_u32_e32 v58, 0x39c8, v30
	v_add_u32_e32 v59, 0x3de0, v30
	v_add_u32_e32 v60, 0x3de8, v30
	s_mov_b32 s15, 0xc3e00000
	v_mov_b32_e32 v61, 0x43e00000
	s_movk_i32 s16, 0x1600
	s_movk_i32 s17, 0xaff
	v_add_u32_e32 v62, 0x400, v75
	v_add_u32_e32 v63, 0x600, v75
	v_mov_b32_e32 v64, v69

.LBB0_191:
	s_or_b64 exec, exec, s[0:1]
	s_cmp_eq_u32 s99, 1
	s_cbranch_scc1 .Lconv_ret_h0
	s_and_saveexec_b64 s[0:1], s[6:7]
	s_cbranch_execz .LBB0_226
	v_mov_b32_e32 v77, 0
	v_lshl_add_u64 v[2:3], s[58:59], 0, v[76:77]
	s_mov_b64 s[6:7], 0x37900000
	v_lshl_add_u64 v[74:75], v[2:3], 0, s[6:7]
	v_lshl_or_b32 v77, s96, 9, v94
	s_lshl_b32 s12, s3, 6
	s_mov_b64 s[6:7], 0
	s_movk_i32 s13, 0x800
	s_movk_i32 s14, 0x3ff
	v_mov_b32_e32 v82, v69
	s_branch .LBB0_194

.LBB0_400:
	s_cmp_lt_i32 s76, 2
	s_cselect_b64 s[6:7], -1, 0
	s_add_u32 s82, s58, 0x32100000
	s_addc_u32 s83, s59, 0
	s_and_b64 s[0:1], s[6:7], s[0:1]
	s_andn2_b64 vcc, exec, s[0:1]
	s_cbranch_vccnz .LBB0_417
	s_mov_b32 s101, s2
	s_cmpk_lt_i32 s96, 192
	s_cbranch_scc1 .Lh0_gemm
	s_sub_i32 s96, s96, 192
	s_sub_i32 s2, s101, 192
	s_mov_b32 s98, 0
	s_mov_b32 s100, 2
	s_mov_b32 s99, 1
	v_readlane_b32 s6, v239, 34
	v_readlane_b32 s7, v239, 35
	s_nop 3
	s_sub_u32 s6, s6, 0x128
	s_subb_u32 s7, s7, 0
	v_writelane_b32 v237, s46, 8
	v_writelane_b32 v237, s47, 9
	v_writelane_b32 v237, s48, 10
	v_writelane_b32 v237, s49, 11
	v_writelane_b32 v237, s50, 12
	v_writelane_b32 v237, s51, 13
	s_load_dwordx2 s[82:83], s[6:7], 0xc8
	s_load_dwordx2 s[46:47], s[6:7], 0x28
	s_load_dwordx2 s[48:49], s[6:7], 0x30
	s_load_dwordx2 s[50:51], s[6:7], 0x38
	s_waitcnt lgkmcnt(0)
	s_branch .Lconv_entry
.Ltr_fwd1:
	s_branch .Ltr_fwd2
.Ltr_bwd1:
	s_branch .Lconv_entry
.Lconv_ret_h0:
	v_readlane_b32 s46, v237, 8
	v_readlane_b32 s47, v237, 9
	v_readlane_b32 s48, v237, 10
	v_readlane_b32 s49, v237, 11
	v_readlane_b32 s50, v237, 12
	v_readlane_b32 s51, v237, 13
	s_mov_b32 s99, 0
	s_add_i32 s96, s96, 192
	s_mov_b32 s2, s101
	s_add_u32 s82, s58, 0x32100000
	s_addc_u32 s83, s59, 0
	s_mov_b64 exec, -1
	s_mov_b64 s[0:1], -1
	s_branch .LBB0_417

.LBB0_702:
	s_add_i32 s22, s22, 1
	s_mov_b64 s[18:19], 0
	s_branch .LBB0_698
.Ltr_fwd2:
	s_branch .Ltr_fwd3
.Ltr_bwd2:
	s_branch .Ltr_bwd1
.LBB0_703:
	global_load_dword v18, v17, s[58:59] offset:512 sc1
	s_waitcnt vmcnt(0)
	v_cmp_eq_u32_e32 vcc, 0, v18
	s_cbranch_vccnz .LBB0_705
	s_branch .LBB0_698

.LBB0_1119:
	s_lshl_b64 s[22:23], s[20:21], 18
	s_add_u32 s21, s31, s22
	s_addc_u32 s28, s33, s23
	s_and_b64 s[22:23], s[6:7], exec
	s_cselect_b32 s23, s28, s27
	s_cselect_b32 s22, s21, s26
	s_add_u32 s24, s24, 0x28080
	s_addc_u32 s25, s25, 0
	s_add_u32 s21, s26, 0x100
	s_addc_u32 s50, s27, 0
	s_mov_b32 s51, -2
	ds_read_b128 v[88:91], v85
	ds_read_b128 v[92:95], v85 offset:1024
	ds_read_b128 v[96:99], v85 offset:2048
	ds_read_b128 v[100:103], v85 offset:3072
	s_add_u32 s26, s24, 0xfffd8080
	s_addc_u32 s27, s25, -1
	s_cmp_eq_u32 s51, 4
	s_cselect_b32 s29, s1, s27
	s_cselect_b32 s28, s0, s26
	s_cselect_b32 s27, s23, s50
	s_cselect_b32 s26, s22, s21
	v_lshl_add_u64 v[136:137], s[24:25], 0, v[76:77]
	s_add_i32 m0, s15, 0xc000
	ds_read_b128 v[104:107], v86
	ds_read_b128 v[108:111], v86 offset:1024
	ds_read_b128 v[112:115], v86 offset:2048
	ds_read_b128 v[116:119], v86 offset:3072
	ds_read_b128 v[120:123], v86 offset:4096
	ds_read_b128 v[124:127], v86 offset:5120
	ds_read_b128 v[128:131], v86 offset:6144
	ds_read_b128 v[132:135], v86 offset:7168
	global_load_lds_dwordx4 v[136:137], off
	v_lshl_add_u64 v[136:137], s[24:25], 0, v[78:79]
	s_add_i32 m0, s15, 0xe000
	s_nop 0
	global_load_lds_dwordx4 v[136:137], off
	s_waitcnt vmcnt(8)
	s_waitcnt lgkmcnt(0)
	s_barrier
	s_setprio 1
	s_waitcnt lgkmcnt(0)
	v_mfma_f32_16x16x32_f16 v[62:65], v[88:91], v[104:107], 0
	v_mfma_f32_16x16x32_f16 v[58:61], v[96:99], v[104:107], 0
	v_mfma_f32_16x16x32_f16 v[54:57], v[88:91], v[112:115], 0
	v_mfma_f32_16x16x32_f16 v[50:53], v[96:99], v[112:115], 0
	v_mfma_f32_16x16x32_f16 v[46:49], v[88:91], v[120:123], 0
	v_mfma_f32_16x16x32_f16 v[42:45], v[96:99], v[120:123], 0
	v_mfma_f32_16x16x32_f16 v[38:41], v[88:91], v[128:131], 0
	v_mfma_f32_16x16x32_f16 v[34:37], v[96:99], v[128:131], 0
	v_mfma_f32_16x16x32_f16 v[62:65], v[92:95], v[108:111], v[62:65]
	v_mfma_f32_16x16x32_f16 v[58:61], v[100:103], v[108:111], v[58:61]
	v_mfma_f32_16x16x32_f16 v[54:57], v[92:95], v[116:119], v[54:57]
	v_mfma_f32_16x16x32_f16 v[50:53], v[100:103], v[116:119], v[50:53]
	s_setprio 2
	s_barrier
	v_mfma_f32_16x16x32_f16 v[46:49], v[92:95], v[124:127], v[46:49]
	v_mfma_f32_16x16x32_f16 v[42:45], v[100:103], v[124:127], v[42:45]
	v_mfma_f32_16x16x32_f16 v[38:41], v[92:95], v[132:135], v[38:41]
	v_mfma_f32_16x16x32_f16 v[34:37], v[100:103], v[132:135], v[34:37]
	s_setprio 0
	s_setprio 1
	s_setprio 0
	s_nop 0
	s_add_i32 s60, s48, s34
	v_lshl_add_u64 v[136:137], s[26:27], 0, v[70:71]
	s_mov_b32 m0, s60
	ds_read_b128 v[104:107], v86 offset:16384
	ds_read_b128 v[108:111], v86 offset:17408
	ds_read_b128 v[112:115], v86 offset:18432
	ds_read_b128 v[116:119], v86 offset:19456
	ds_read_b128 v[120:123], v86 offset:20480
	ds_read_b128 v[124:127], v86 offset:21504
	ds_read_b128 v[128:131], v86 offset:22528
	ds_read_b128 v[132:135], v86 offset:23552
	global_load_lds_dwordx4 v[136:137], off
	s_add_i32 m0, s60, 0x2000
	s_add_u32 s60, s26, 0x20000
	v_lshl_add_u64 v[138:139], s[26:27], 0, v[66:67]
	s_addc_u32 s61, s27, 0
	global_load_lds_dwordx4 v[138:139], off
	v_lshl_add_u64 v[140:141], s[60:61], 0, v[70:71]
	s_mov_b32 m0, s35
	v_lshl_add_u64 v[142:143], s[28:29], 0, v[68:69]
	global_load_lds_dwordx4 v[140:141], off
	v_lshl_add_u64 v[140:141], s[60:61], 0, v[66:67]
	s_mov_b32 m0, s36
	s_nop 0
	global_load_lds_dwordx4 v[140:141], off
	v_lshl_add_u64 v[140:141], s[28:29], 0, v[72:73]
	s_mov_b32 m0, s15
	s_nop 0
	global_load_lds_dwordx4 v[140:141], off
	s_mov_b32 m0, s37
	s_nop 0
	global_load_lds_dwordx4 v[142:143], off
	s_waitcnt vmcnt(8)
	s_waitcnt lgkmcnt(0)
	s_barrier
	s_setprio 1
	s_waitcnt lgkmcnt(0)
	v_mfma_f32_16x16x32_f16 v[30:33], v[88:91], v[104:107], 0
	v_mfma_f32_16x16x32_f16 v[26:29], v[96:99], v[104:107], 0
	v_mfma_f32_16x16x32_f16 v[22:25], v[88:91], v[112:115], 0
	v_mfma_f32_16x16x32_f16 v[18:21], v[96:99], v[112:115], 0
	v_mfma_f32_16x16x32_f16 v[14:17], v[88:91], v[120:123], 0
	v_mfma_f32_16x16x32_f16 v[10:13], v[96:99], v[120:123], 0
	v_mfma_f32_16x16x32_f16 v[6:9], v[88:91], v[128:131], 0
	v_mfma_f32_16x16x32_f16 v[2:5], v[96:99], v[128:131], 0
	v_mfma_f32_16x16x32_f16 v[30:33], v[92:95], v[108:111], v[30:33]
	v_mfma_f32_16x16x32_f16 v[26:29], v[100:103], v[108:111], v[26:29]
	v_mfma_f32_16x16x32_f16 v[22:25], v[92:95], v[116:119], v[22:25]
	v_mfma_f32_16x16x32_f16 v[18:21], v[100:103], v[116:119], v[18:21]
	s_setprio 2
	s_barrier
	v_mfma_f32_16x16x32_f16 v[14:17], v[92:95], v[124:127], v[14:17]
	v_mfma_f32_16x16x32_f16 v[10:13], v[100:103], v[124:127], v[10:13]
	v_mfma_f32_16x16x32_f16 v[6:9], v[92:95], v[132:135], v[6:9]
	v_mfma_f32_16x16x32_f16 v[2:5], v[100:103], v[132:135], v[2:5]
	s_setprio 0
	s_setprio 1
	s_setprio 0
	s_nop 0
	s_add_i32 s60, 0, 0x18000
	v_add_u32_e32 v87, s60, v84
	ds_read_b128 v[88:91], v87
	ds_read_b128 v[92:95], v87 offset:1024
	ds_read_b128 v[96:99], v87 offset:2048
	ds_read_b128 v[100:103], v87 offset:3072
	s_add_u32 s28, s28, 0x28000
	s_addc_u32 s29, s29, 0
	s_mov_b32 m0, s38
	v_lshl_add_u64 v[144:145], s[28:29], 0, v[72:73]
	ds_read_b128 v[104:107], v86 offset:32768
	ds_read_b128 v[108:111], v86 offset:33792
	ds_read_b128 v[112:115], v86 offset:34816
	ds_read_b128 v[116:119], v86 offset:35840
	ds_read_b128 v[120:123], v86 offset:36864
	ds_read_b128 v[124:127], v86 offset:37888
	ds_read_b128 v[128:131], v86 offset:38912
	ds_read_b128 v[132:135], v86 offset:39936
	global_load_lds_dwordx4 v[144:145], off
	v_lshl_add_u64 v[144:145], s[28:29], 0, v[68:69]
	s_mov_b32 m0, s39
	s_nop 0
	global_load_lds_dwordx4 v[144:145], off
	s_waitcnt vmcnt(8)
	s_waitcnt lgkmcnt(0)
	s_barrier
	s_setprio 1
	s_waitcnt lgkmcnt(0)
	v_mfma_f32_16x16x32_f16 v[62:65], v[88:91], v[104:107], v[62:65]
	v_mfma_f32_16x16x32_f16 v[58:61], v[96:99], v[104:107], v[58:61]
	v_mfma_f32_16x16x32_f16 v[54:57], v[88:91], v[112:115], v[54:57]
	v_mfma_f32_16x16x32_f16 v[50:53], v[96:99], v[112:115], v[50:53]
	v_mfma_f32_16x16x32_f16 v[46:49], v[88:91], v[120:123], v[46:49]
	v_mfma_f32_16x16x32_f16 v[42:45], v[96:99], v[120:123], v[42:45]
	v_mfma_f32_16x16x32_f16 v[38:41], v[88:91], v[128:131], v[38:41]
	v_mfma_f32_16x16x32_f16 v[34:37], v[96:99], v[128:131], v[34:37]
	v_mfma_f32_16x16x32_f16 v[62:65], v[92:95], v[108:111], v[62:65]
	v_mfma_f32_16x16x32_f16 v[58:61], v[100:103], v[108:111], v[58:61]
	v_mfma_f32_16x16x32_f16 v[54:57], v[92:95], v[116:119], v[54:57]
	v_mfma_f32_16x16x32_f16 v[50:53], v[100:103], v[116:119], v[50:53]
	s_setprio 2
	s_barrier
	v_mfma_f32_16x16x32_f16 v[46:49], v[92:95], v[124:127], v[46:49]
	v_mfma_f32_16x16x32_f16 v[42:45], v[100:103], v[124:127], v[42:45]
	v_mfma_f32_16x16x32_f16 v[38:41], v[92:95], v[132:135], v[38:41]
	v_mfma_f32_16x16x32_f16 v[34:37], v[100:103], v[132:135], v[34:37]
	s_setprio 0
	s_setprio 1
	s_setprio 0
	s_nop 0
	s_add_i32 s28, s60, s34
	v_lshl_add_u64 v[136:137], v[136:137], 0, s[16:17]
	s_mov_b32 m0, s28
	ds_read_b128 v[104:107], v86 offset:49152
	ds_read_b128 v[108:111], v86 offset:50176
	ds_read_b128 v[112:115], v86 offset:51200
	ds_read_b128 v[116:119], v86 offset:52224
	ds_read_b128 v[120:123], v86 offset:53248
	ds_read_b128 v[124:127], v86 offset:54272
	ds_read_b128 v[128:131], v86 offset:55296
	ds_read_b128 v[132:135], v86 offset:56320
	global_load_lds_dwordx4 v[136:137], off
	s_add_i32 m0, s28, 0x2000
	s_add_u32 s26, s26, 0x20080
	v_lshl_add_u64 v[136:137], v[138:139], 0, s[16:17]
	s_addc_u32 s27, s27, 0
	global_load_lds_dwordx4 v[136:137], off
	v_lshl_add_u64 v[136:137], s[26:27], 0, v[70:71]
	s_mov_b32 m0, s45
	s_nop 0
	global_load_lds_dwordx4 v[136:137], off
	v_lshl_add_u64 v[136:137], s[26:27], 0, v[66:67]
	s_mov_b32 m0, s46
	s_nop 0
	global_load_lds_dwordx4 v[136:137], off
	v_lshl_add_u64 v[136:137], v[140:141], 0, s[16:17]
	s_mov_b32 m0, s43
	s_nop 0
	global_load_lds_dwordx4 v[136:137], off
	v_lshl_add_u64 v[136:137], v[142:143], 0, s[16:17]
	s_mov_b32 m0, s44
	s_nop 0
	global_load_lds_dwordx4 v[136:137], off
	s_waitcnt vmcnt(8)
	s_waitcnt lgkmcnt(0)
	s_barrier
	s_setprio 1
	s_waitcnt lgkmcnt(0)
	v_mfma_f32_16x16x32_f16 v[30:33], v[88:91], v[104:107], v[30:33]
	v_mfma_f32_16x16x32_f16 v[26:29], v[96:99], v[104:107], v[26:29]
	v_mfma_f32_16x16x32_f16 v[22:25], v[88:91], v[112:115], v[22:25]
	v_mfma_f32_16x16x32_f16 v[18:21], v[96:99], v[112:115], v[18:21]
	v_mfma_f32_16x16x32_f16 v[14:17], v[88:91], v[120:123], v[14:17]
	v_mfma_f32_16x16x32_f16 v[10:13], v[96:99], v[120:123], v[10:13]
	v_mfma_f32_16x16x32_f16 v[6:9], v[88:91], v[128:131], v[6:9]
	v_mfma_f32_16x16x32_f16 v[2:5], v[96:99], v[128:131], v[2:5]
	v_mfma_f32_16x16x32_f16 v[30:33], v[92:95], v[108:111], v[30:33]
	v_mfma_f32_16x16x32_f16 v[26:29], v[100:103], v[108:111], v[26:29]
	v_mfma_f32_16x16x32_f16 v[22:25], v[92:95], v[116:119], v[22:25]
	v_mfma_f32_16x16x32_f16 v[18:21], v[100:103], v[116:119], v[18:21]
	s_setprio 2
	s_barrier
	v_mfma_f32_16x16x32_f16 v[14:17], v[92:95], v[124:127], v[14:17]
	v_mfma_f32_16x16x32_f16 v[10:13], v[100:103], v[124:127], v[10:13]
	v_mfma_f32_16x16x32_f16 v[6:9], v[92:95], v[132:135], v[6:9]
	v_mfma_f32_16x16x32_f16 v[2:5], v[100:103], v[132:135], v[2:5]
	s_setprio 0
	s_setprio 1
	s_setprio 0
	s_nop 0
	s_add_i32 s51, s51, 2
	s_add_u32 s24, s24, 0x100
	s_addc_u32 s25, s25, 0
	s_add_u32 s21, s21, 0x100
	s_addc_u32 s50, s50, 0
	s_cmp_gt_u32 s51, 5
	s_cbranch_scc0 .LBB0_1120
	s_branch .Lpeel_exit_5
.Ltr_fwd3:
	s_branch .Lconv_ret_rec
.Ltr_bwd3:
	s_branch .Ltr_bwd2
.LBB0_1120:
	ds_read_b128 v[88:91], v85
	ds_read_b128 v[92:95], v85 offset:1024
	ds_read_b128 v[96:99], v85 offset:2048
	ds_read_b128 v[100:103], v85 offset:3072
	s_add_u32 s26, s24, 0xfffd8080
	s_addc_u32 s27, s25, -1
	s_cmp_eq_u32 s51, 4
	s_cselect_b32 s29, s1, s27
	s_cselect_b32 s28, s0, s26
	s_cselect_b32 s27, s23, s50
	s_cselect_b32 s26, s22, s21
	v_lshl_add_u64 v[136:137], s[24:25], 0, v[76:77]
	s_add_i32 m0, s15, 0xc000
	ds_read_b128 v[104:107], v86
	ds_read_b128 v[108:111], v86 offset:1024
	ds_read_b128 v[112:115], v86 offset:2048
	ds_read_b128 v[116:119], v86 offset:3072
	ds_read_b128 v[120:123], v86 offset:4096
	ds_read_b128 v[124:127], v86 offset:5120
	ds_read_b128 v[128:131], v86 offset:6144
	ds_read_b128 v[132:135], v86 offset:7168
	global_load_lds_dwordx4 v[136:137], off
	v_lshl_add_u64 v[136:137], s[24:25], 0, v[78:79]
	s_add_i32 m0, s15, 0xe000
	s_nop 0
	global_load_lds_dwordx4 v[136:137], off
	s_waitcnt vmcnt(8)
	s_waitcnt lgkmcnt(0)
	s_barrier
	s_setprio 1
	s_waitcnt lgkmcnt(0)
	v_mfma_f32_16x16x32_f16 v[62:65], v[88:91], v[104:107], v[62:65]
	v_mfma_f32_16x16x32_f16 v[58:61], v[96:99], v[104:107], v[58:61]
	v_mfma_f32_16x16x32_f16 v[54:57], v[88:91], v[112:115], v[54:57]
	v_mfma_f32_16x16x32_f16 v[50:53], v[96:99], v[112:115], v[50:53]
	v_mfma_f32_16x16x32_f16 v[46:49], v[88:91], v[120:123], v[46:49]
	v_mfma_f32_16x16x32_f16 v[42:45], v[96:99], v[120:123], v[42:45]
	v_mfma_f32_16x16x32_f16 v[38:41], v[88:91], v[128:131], v[38:41]
	v_mfma_f32_16x16x32_f16 v[34:37], v[96:99], v[128:131], v[34:37]
	v_mfma_f32_16x16x32_f16 v[62:65], v[92:95], v[108:111], v[62:65]
	v_mfma_f32_16x16x32_f16 v[58:61], v[100:103], v[108:111], v[58:61]
	v_mfma_f32_16x16x32_f16 v[54:57], v[92:95], v[116:119], v[54:57]
	v_mfma_f32_16x16x32_f16 v[50:53], v[100:103], v[116:119], v[50:53]
	s_setprio 2
	s_barrier
	v_mfma_f32_16x16x32_f16 v[46:49], v[92:95], v[124:127], v[46:49]
	v_mfma_f32_16x16x32_f16 v[42:45], v[100:103], v[124:127], v[42:45]
	v_mfma_f32_16x16x32_f16 v[38:41], v[92:95], v[132:135], v[38:41]
	v_mfma_f32_16x16x32_f16 v[34:37], v[100:103], v[132:135], v[34:37]
	s_setprio 0
	s_setprio 1
	s_setprio 0
	s_nop 0
	s_add_i32 s60, s48, s34
	v_lshl_add_u64 v[136:137], s[26:27], 0, v[70:71]
	s_mov_b32 m0, s60
	ds_read_b128 v[104:107], v86 offset:16384
	ds_read_b128 v[108:111], v86 offset:17408
	ds_read_b128 v[112:115], v86 offset:18432
	ds_read_b128 v[116:119], v86 offset:19456
	ds_read_b128 v[120:123], v86 offset:20480
	ds_read_b128 v[124:127], v86 offset:21504
	ds_read_b128 v[128:131], v86 offset:22528
	ds_read_b128 v[132:135], v86 offset:23552
	global_load_lds_dwordx4 v[136:137], off
	s_add_i32 m0, s60, 0x2000
	s_add_u32 s60, s26, 0x20000
	v_lshl_add_u64 v[138:139], s[26:27], 0, v[66:67]
	s_addc_u32 s61, s27, 0
	global_load_lds_dwordx4 v[138:139], off
	v_lshl_add_u64 v[140:141], s[60:61], 0, v[70:71]
	s_mov_b32 m0, s35
	v_lshl_add_u64 v[142:143], s[28:29], 0, v[68:69]
	global_load_lds_dwordx4 v[140:141], off
	v_lshl_add_u64 v[140:141], s[60:61], 0, v[66:67]
	s_mov_b32 m0, s36
	s_nop 0
	global_load_lds_dwordx4 v[140:141], off
	v_lshl_add_u64 v[140:141], s[28:29], 0, v[72:73]
	s_mov_b32 m0, s15
	s_nop 0
	global_load_lds_dwordx4 v[140:141], off
	s_mov_b32 m0, s37
	s_nop 0
	global_load_lds_dwordx4 v[142:143], off
	s_waitcnt vmcnt(8)
	s_waitcnt lgkmcnt(0)
	s_barrier
	s_setprio 1
	s_waitcnt lgkmcnt(0)
	v_mfma_f32_16x16x32_f16 v[30:33], v[88:91], v[104:107], v[30:33]
	v_mfma_f32_16x16x32_f16 v[26:29], v[96:99], v[104:107], v[26:29]
	v_mfma_f32_16x16x32_f16 v[22:25], v[88:91], v[112:115], v[22:25]
	v_mfma_f32_16x16x32_f16 v[18:21], v[96:99], v[112:115], v[18:21]
	v_mfma_f32_16x16x32_f16 v[14:17], v[88:91], v[120:123], v[14:17]
	v_mfma_f32_16x16x32_f16 v[10:13], v[96:99], v[120:123], v[10:13]
	v_mfma_f32_16x16x32_f16 v[6:9], v[88:91], v[128:131], v[6:9]
	v_mfma_f32_16x16x32_f16 v[2:5], v[96:99], v[128:131], v[2:5]
	v_mfma_f32_16x16x32_f16 v[30:33], v[92:95], v[108:111], v[30:33]
	v_mfma_f32_16x16x32_f16 v[26:29], v[100:103], v[108:111], v[26:29]
	v_mfma_f32_16x16x32_f16 v[22:25], v[92:95], v[116:119], v[22:25]
	v_mfma_f32_16x16x32_f16 v[18:21], v[100:103], v[116:119], v[18:21]
	s_setprio 2
	s_barrier
	v_mfma_f32_16x16x32_f16 v[14:17], v[92:95], v[124:127], v[14:17]
	v_mfma_f32_16x16x32_f16 v[10:13], v[100:103], v[124:127], v[10:13]
	v_mfma_f32_16x16x32_f16 v[6:9], v[92:95], v[132:135], v[6:9]
	v_mfma_f32_16x16x32_f16 v[2:5], v[100:103], v[132:135], v[2:5]
	s_setprio 0
	s_setprio 1
	s_setprio 0
	s_nop 0
	s_add_i32 s60, 0, 0x18000
	v_add_u32_e32 v87, s60, v84
	ds_read_b128 v[88:91], v87
	ds_read_b128 v[92:95], v87 offset:1024
	ds_read_b128 v[96:99], v87 offset:2048
	ds_read_b128 v[100:103], v87 offset:3072
	s_add_u32 s28, s28, 0x28000
	s_addc_u32 s29, s29, 0
	s_mov_b32 m0, s38
	v_lshl_add_u64 v[144:145], s[28:29], 0, v[72:73]
	ds_read_b128 v[104:107], v86 offset:32768
	ds_read_b128 v[108:111], v86 offset:33792
	ds_read_b128 v[112:115], v86 offset:34816
	ds_read_b128 v[116:119], v86 offset:35840
	ds_read_b128 v[120:123], v86 offset:36864
	ds_read_b128 v[124:127], v86 offset:37888
	ds_read_b128 v[128:131], v86 offset:38912
	ds_read_b128 v[132:135], v86 offset:39936
	global_load_lds_dwordx4 v[144:145], off
	v_lshl_add_u64 v[144:145], s[28:29], 0, v[68:69]
	s_mov_b32 m0, s39
	s_nop 0
	global_load_lds_dwordx4 v[144:145], off
	s_waitcnt vmcnt(8)
	s_waitcnt lgkmcnt(0)
	s_barrier
	s_setprio 1
	s_waitcnt lgkmcnt(0)
	v_mfma_f32_16x16x32_f16 v[62:65], v[88:91], v[104:107], v[62:65]
	v_mfma_f32_16x16x32_f16 v[58:61], v[96:99], v[104:107], v[58:61]
	v_mfma_f32_16x16x32_f16 v[54:57], v[88:91], v[112:115], v[54:57]
	v_mfma_f32_16x16x32_f16 v[50:53], v[96:99], v[112:115], v[50:53]
	v_mfma_f32_16x16x32_f16 v[46:49], v[88:91], v[120:123], v[46:49]
	v_mfma_f32_16x16x32_f16 v[42:45], v[96:99], v[120:123], v[42:45]
	v_mfma_f32_16x16x32_f16 v[38:41], v[88:91], v[128:131], v[38:41]
	v_mfma_f32_16x16x32_f16 v[34:37], v[96:99], v[128:131], v[34:37]
	v_mfma_f32_16x16x32_f16 v[62:65], v[92:95], v[108:111], v[62:65]
	v_mfma_f32_16x16x32_f16 v[58:61], v[100:103], v[108:111], v[58:61]
	v_mfma_f32_16x16x32_f16 v[54:57], v[92:95], v[116:119], v[54:57]
	v_mfma_f32_16x16x32_f16 v[50:53], v[100:103], v[116:119], v[50:53]
	s_setprio 2
	s_barrier
	v_mfma_f32_16x16x32_f16 v[46:49], v[92:95], v[124:127], v[46:49]
	v_mfma_f32_16x16x32_f16 v[42:45], v[100:103], v[124:127], v[42:45]
	v_mfma_f32_16x16x32_f16 v[38:41], v[92:95], v[132:135], v[38:41]
	v_mfma_f32_16x16x32_f16 v[34:37], v[100:103], v[132:135], v[34:37]
	s_setprio 0
	s_setprio 1
	s_setprio 0
	s_nop 0
	s_add_i32 s28, s60, s34
	v_lshl_add_u64 v[136:137], v[136:137], 0, s[16:17]
	s_mov_b32 m0, s28
	ds_read_b128 v[104:107], v86 offset:49152
	ds_read_b128 v[108:111], v86 offset:50176
	ds_read_b128 v[112:115], v86 offset:51200
	ds_read_b128 v[116:119], v86 offset:52224
	ds_read_b128 v[120:123], v86 offset:53248
	ds_read_b128 v[124:127], v86 offset:54272
	ds_read_b128 v[128:131], v86 offset:55296
	ds_read_b128 v[132:135], v86 offset:56320
	global_load_lds_dwordx4 v[136:137], off
	s_add_i32 m0, s28, 0x2000
	s_add_u32 s26, s26, 0x20080
	v_lshl_add_u64 v[136:137], v[138:139], 0, s[16:17]
	s_addc_u32 s27, s27, 0
	global_load_lds_dwordx4 v[136:137], off
	v_lshl_add_u64 v[136:137], s[26:27], 0, v[70:71]
	s_mov_b32 m0, s45
	s_nop 0
	global_load_lds_dwordx4 v[136:137], off
	v_lshl_add_u64 v[136:137], s[26:27], 0, v[66:67]
	s_mov_b32 m0, s46
	s_nop 0
	global_load_lds_dwordx4 v[136:137], off
	v_lshl_add_u64 v[136:137], v[140:141], 0, s[16:17]
	s_mov_b32 m0, s43
	s_nop 0
	global_load_lds_dwordx4 v[136:137], off
	v_lshl_add_u64 v[136:137], v[142:143], 0, s[16:17]
	s_mov_b32 m0, s44
	s_nop 0
	global_load_lds_dwordx4 v[136:137], off
	s_waitcnt vmcnt(8)
	s_waitcnt lgkmcnt(0)
	s_barrier
	s_setprio 1
	s_waitcnt lgkmcnt(0)
	v_mfma_f32_16x16x32_f16 v[30:33], v[88:91], v[104:107], v[30:33]
	v_mfma_f32_16x16x32_f16 v[26:29], v[96:99], v[104:107], v[26:29]
	v_mfma_f32_16x16x32_f16 v[22:25], v[88:91], v[112:115], v[22:25]
	v_mfma_f32_16x16x32_f16 v[18:21], v[96:99], v[112:115], v[18:21]
	v_mfma_f32_16x16x32_f16 v[14:17], v[88:91], v[120:123], v[14:17]
	v_mfma_f32_16x16x32_f16 v[10:13], v[96:99], v[120:123], v[10:13]
	v_mfma_f32_16x16x32_f16 v[6:9], v[88:91], v[128:131], v[6:9]
	v_mfma_f32_16x16x32_f16 v[2:5], v[96:99], v[128:131], v[2:5]
	v_mfma_f32_16x16x32_f16 v[30:33], v[92:95], v[108:111], v[30:33]
	v_mfma_f32_16x16x32_f16 v[26:29], v[100:103], v[108:111], v[26:29]
	v_mfma_f32_16x16x32_f16 v[22:25], v[92:95], v[116:119], v[22:25]
	v_mfma_f32_16x16x32_f16 v[18:21], v[100:103], v[116:119], v[18:21]
	s_setprio 2
	s_barrier
	v_mfma_f32_16x16x32_f16 v[14:17], v[92:95], v[124:127], v[14:17]
	v_mfma_f32_16x16x32_f16 v[10:13], v[100:103], v[124:127], v[10:13]
	v_mfma_f32_16x16x32_f16 v[6:9], v[92:95], v[132:135], v[6:9]
	v_mfma_f32_16x16x32_f16 v[2:5], v[100:103], v[132:135], v[2:5]
	s_setprio 0
	s_setprio 1
	s_setprio 0
	s_nop 0
	s_add_i32 s51, s51, 2
	s_add_u32 s24, s24, 0x100
	s_addc_u32 s25, s25, 0
	s_add_u32 s21, s21, 0x100
	s_addc_u32 s50, s50, 0
	s_cmp_gt_u32 s51, 5
	s_cbranch_scc0 .LBB0_1120

.LBB0_1568:
	s_and_b64 vcc, exec, s[0:1]
	s_cbranch_vccz .LBB0_1579
	s_cmpk_lt_i32 s96, 64
	s_cbranch_scc1 .LBB0_1579
	s_cmpk_lt_i32 s96, 80
	s_cbranch_scc1 .Lrec_spare_a
	s_cmpk_lt_i32 s96, 230
	s_cbranch_scc1 .Lrec_conv
	v_writelane_b32 v237, s2, 0
	v_writelane_b32 v237, s96, 1
	v_writelane_b32 v237, s8, 2
	v_writelane_b32 v237, s9, 3
	s_sub_i32 s96, s96, 230
	s_branch .Lrec_spare_go
.Lrec_spare_a:
	v_writelane_b32 v237, s2, 0
	v_writelane_b32 v237, s96, 1
	v_writelane_b32 v237, s8, 2
	v_writelane_b32 v237, s9, 3
	s_sub_i32 s96, s96, 38
.Lrec_spare_go:
	s_movk_i32 s2, 42
	s_mov_b32 s98, 2
	s_mov_b32 s100, 3
	s_mov_b32 s99, 2
	s_waitcnt vmcnt(0) lgkmcnt(0)
	s_branch .Ltr_bwd3
.Lconv_ret_rec:
	s_mov_b32 s99, 0
	s_mov_b64 exec, -1
	v_readlane_b32 s2, v237, 0
	v_readlane_b32 s96, v237, 1
	v_readlane_b32 s8, v237, 2
	v_readlane_b32 s9, v237, 3
	s_nop 3
	s_branch .LBB0_1579
.Lrec_conv:
	s_lshl_b32 s0, s96, 3
	s_addk_i32 s0, 0xfd80
	v_or_b32_e32 v1, s0, v186
	s_movk_i32 s0, 0x4200
	s_waitcnt vmcnt(0)
	v_and_b32_e32 v3, 7, v0
	v_mad_u32_u24 v6, v186, s0, 0
	s_movk_i32 s0, 0xe00
	v_bfe_u32 v18, v0, 3, 3
	v_lshlrev_b32_e32 v2, 4, v3
	v_mul_u32_u24_e32 v9, 0x840, v3
	v_mov_b32_e32 v3, 0
	s_lshl_b32 s3, s2, 3
	v_cmp_gt_i32_e64 s[4:5], s0, v1
	v_add_u32_e32 v7, v6, v2
	v_mul_u32_u24_e32 v8, 0x84, v18
	v_lshl_add_u64 v[4:5], s[58:59], 0, v[2:3]
	s_mov_b64 s[0:1], 0x100000
	s_mov_b32 s21, 0xe0000
	s_movk_i32 s3, 0x4b0
	v_lshl_add_u64 v[26:27], v[4:5], 0, s[0:1]
	v_lshlrev_b32_e32 v10, 2, v18
	s_mov_b64 s[0:1], 0x1c100000
	v_lshl_add_u64 v[30:31], s[90:91], 0, v[2:3]
	v_lshl_add_u64 v[32:33], s[92:93], 0, v[2:3]
	v_lshl_add_u64 v[34:35], s[94:95], 0, v[2:3]
	v_mul_u32_u24_e32 v2, 0x1c00, v18
	v_mul_lo_u32 v3, v1, s21
	v_add_u32_e32 v25, v7, v8
	s_mov_b32 s7, 0
	v_or_b32_e32 v20, 8, v18
	v_or_b32_e32 v22, 16, v18
	v_or_b32_e32 v24, 24, v18
	v_add3_u32 v19, v6, v9, v10
	v_lshl_add_u64 v[28:29], v[4:5], 0, s[0:1]
	s_movk_i32 s20, 0x1c00
	s_mov_b64 s[14:15], 3
	s_mov_b32 s98, 3
	s_mov_b64 s[10:11], 0
	v_or_b32_e32 v21, v2, v3
	s_mul_i32 s22, s3, 0xe0000
	v_lshlrev_b32_e32 v23, 7, v1
	s_lshl_b32 s23, s3, 7
	s_movk_i32 s24, 0x60
	s_mov_b32 s25, 0xff200000
	s_mov_b32 s26, 0x38000
	s_mov_b32 s27, 0x70000
	s_mov_b32 s28, 0xa8000
	s_mov_b32 s29, 0x118000
	s_mov_b32 s30, 0x150000
	s_mov_b32 s31, 0x188000
	s_mov_b32 s33, 0x1c0000
	s_mov_b32 s34, 0x1f8000
	s_mov_b32 s35, 0x230000
	s_mov_b32 s36, 0x268000
	s_mov_b32 s37, 0x2a0000
	s_mov_b32 s38, 0x2d8000
	s_mov_b32 s39, 0x310000
	s_mov_b32 s40, 0x348000
	v_add_u32_e32 v39, 0x420, v25
	v_add_u32_e32 v48, 0x428, v25
	v_add_u32_e32 v49, 0x840, v25
	v_add_u32_e32 v50, 0x848, v25
	v_add_u32_e32 v51, 0xc60, v25
	v_add_u32_e32 v52, 0xc68, v25
	v_add_u32_e32 v53, 0x1080, v25
	v_add_u32_e32 v54, 0x1088, v25
	v_add_u32_e32 v55, 0x14a0, v25
	v_add_u32_e32 v56, 0x14a8, v25
	v_add_u32_e32 v57, 0x18c0, v25
	v_add_u32_e32 v58, 0x18c8, v25
	v_add_u32_e32 v59, 0x1ce0, v25
	v_add_u32_e32 v60, 0x1ce8, v25
	v_add_u32_e32 v61, 0x2100, v25
	v_add_u32_e32 v62, 0x2108, v25
	v_add_u32_e32 v63, 0x2520, v25
	v_add_u32_e32 v64, 0x2528, v25
	v_add_u32_e32 v65, 0x2940, v25
	v_add_u32_e32 v66, 0x2948, v25
	v_add_u32_e32 v67, 0x2d60, v25
	v_add_u32_e32 v68, 0x2d68, v25
	s_mov_b32 s41, 0xc3e00000
	s_movk_i32 s42, 0xdff
	s_mov_b32 s43, 0x92492493
	s_movk_i32 s44, 0xe400
	v_add_u32_e32 v69, 0x3180, v25
	v_add_u32_e32 v70, 0x3188, v25
	v_add_u32_e32 v71, 0x35a0, v25
	v_add_u32_e32 v72, 0x35a8, v25
	v_add_u32_e32 v73, 0x39c0, v25
	v_add_u32_e32 v74, 0x39c8, v25
	v_mov_b32_e32 v75, 0x43e00000
	s_branch .LBB0_1572
